# accumulator clearing between GEMM units with 64-bit moves (64 instead of 128 instructions per unit)
# speedup vs baseline: 1.0118x; 1.0023x over previous
; #define PG8_BAR __builtin_amdgcn_s_barrier()
; template <int K, bool PERM, bool GATHER, int MODE  , class Sched, class Epi>
; __device__ __forceinline__ void gemm_phase(LAS unsigned char* lds, const Sched& S, const Epi& E, const LAS int* gtab, int wv) {
;     ...
;         if (!has_next) break;
; #pragma unroll
;         for (int a = 0; a < 2; ++a)
; #pragma unroll
;             for (int b = 0; b < 2; ++b)
; #pragma unroll
;                 for (int m = 0; m < 4; ++m)
; #pragma unroll
;                     for (int n = 0; n < 2; ++n) acc[a][b][m][n] = (f32x4){0.f, 0.f, 0.f, 0.f};
;         pmt = cur.r0 >> 8; cur = nxt; cA = nA; cB = nB; ++ui;
;         if (wr == 1) PG8_BAR;
.LBB0_178:
	s_add_u32 s6, s6, 0x20080
	s_addc_u32 s7, s7, 0
	s_add_u32 s73, s8, 0x100
	v_mov_b32_e32 v0, 0
	s_addc_u32 s74, s9, 0
	s_mov_b32 s75, -2
	v_mov_b32_e32 v1, v0
	s_waitcnt lgkmcnt(0)
	v_mov_b64_e32 v[2:3], 0
	v_mov_b64_e32 v[4:5], 0
	v_mov_b64_e32 v[6:7], 0
	v_mov_b64_e32 v[16:17], 0
	v_mov_b64_e32 v[18:19], 0
	v_mov_b64_e32 v[20:21], 0
	v_mov_b64_e32 v[22:23], 0
	v_mov_b64_e32 v[32:33], 0
	v_mov_b64_e32 v[34:35], 0
	v_mov_b64_e32 v[36:37], 0
	v_mov_b64_e32 v[38:39], 0
	v_mov_b64_e32 v[48:49], 0
	v_mov_b64_e32 v[50:51], 0
	v_mov_b64_e32 v[52:53], 0
	v_mov_b64_e32 v[54:55], 0
	v_mov_b64_e32 v[8:9], 0
	v_mov_b64_e32 v[10:11], 0
	v_mov_b64_e32 v[12:13], 0
	v_mov_b64_e32 v[14:15], 0
	v_mov_b64_e32 v[24:25], 0
	v_mov_b64_e32 v[26:27], 0
	v_mov_b64_e32 v[28:29], 0
	v_mov_b64_e32 v[30:31], 0
	v_mov_b64_e32 v[40:41], 0
	v_mov_b64_e32 v[42:43], 0
	v_mov_b64_e32 v[44:45], 0
	v_mov_b64_e32 v[46:47], 0
	v_mov_b64_e32 v[64:65], 0
	v_mov_b64_e32 v[66:67], 0
	v_mov_b64_e32 v[68:69], 0
	v_mov_b64_e32 v[70:71], 0
	v_mov_b64_e32 v[80:81], 0
	v_mov_b64_e32 v[82:83], 0
	v_mov_b64_e32 v[84:85], 0
	v_mov_b64_e32 v[86:87], 0
	v_mov_b64_e32 v[96:97], 0
	v_mov_b64_e32 v[98:99], 0
	v_mov_b64_e32 v[100:101], 0
	v_mov_b64_e32 v[102:103], 0
	v_mov_b64_e32 v[112:113], 0
	v_mov_b64_e32 v[114:115], 0
	v_mov_b64_e32 v[116:117], 0
	v_mov_b64_e32 v[118:119], 0
	v_mov_b64_e32 v[128:129], 0
	v_mov_b64_e32 v[130:131], 0
	v_mov_b64_e32 v[132:133], 0
	v_mov_b64_e32 v[134:135], 0
	v_mov_b64_e32 v[88:89], 0
	v_mov_b64_e32 v[90:91], 0
	v_mov_b64_e32 v[92:93], 0
	v_mov_b64_e32 v[94:95], 0
	v_mov_b64_e32 v[104:105], 0
	v_mov_b64_e32 v[106:107], 0
	v_mov_b64_e32 v[108:109], 0
	v_mov_b64_e32 v[110:111], 0
	v_mov_b64_e32 v[120:121], 0
	v_mov_b64_e32 v[122:123], 0
	v_mov_b64_e32 v[124:125], 0
	v_mov_b64_e32 v[126:127], 0
	v_mov_b64_e32 v[136:137], 0
	v_mov_b64_e32 v[138:139], 0
	v_mov_b64_e32 v[140:141], 0
	v_mov_b64_e32 v[142:143], 0

; #define PG8_STAGE_B(bufoff, gbase) do { _Pragma("unroll") for (int _i = 0; _i < 2; ++_i) { unsigned _o = voffB[_i]; asm volatile("" : "+v"(_o)); \
;         __builtin_amdgcn_global_load_lds((const unsigned*)((const char*)(gbase) + _o), (LAS unsigned*)(lds + (bufoff) + ldsw + _i * 8192), 16, 0, 0); } } while (0)
; #define PG8_STAGE_A(bufoff, gbase, h) do { _Pragma("unroll") for (int _i = 0; _i < 2; ++_i) { unsigned _o = (GATHER ? aoffs[h][_i] : voffA[_i]); asm volatile("" : "+v"(_o)); \
;         __builtin_amdgcn_global_load_lds((const unsigned*)((const char*)(gbase) + _o), (LAS unsigned*)(lds + (bufoff) + ldsw + _i * 8192), 16, 0, 0); } } while (0)
; #define PG8_GOFFS(u) do { if constexpr (GATHER) { _Pragma("unroll") for (int _i = 0; _i < 2; ++_i) { int _R, _C; stage_rc(tid * 16 + _i * 8192, _R, _C); \
;         aoffs[0][_i] = (unsigned)gtab[(u) * 256 + _R] * (unsigned)(K * ES) + (unsigned)(_C * 2); aoffs[1][_i] = (unsigned)gtab[(u) * 256 + 128 + _R] * (unsigned)(K * ES) + (unsigned)(_C * 2); } } } while (0)
; #define PG8_WAIT_V(n) asm volatile("s_waitcnt vmcnt(" #n ")" ::: "memory")
; #define PG8_BAR __builtin_amdgcn_s_barrier()
; template <int K, bool PERM, bool GATHER, int MODE  , class Sched, class Epi>
; __device__ __forceinline__ void gemm_phase(LAS unsigned char* lds, const Sched& S, const Epi& E, const LAS int* gtab, int wv) {
;     ...
;     f32x4 acc[2][2][4][2];
; #pragma unroll
;     for (int a = 0; a < 2; ++a)
; #pragma unroll
;         for (int b = 0; b < 2; ++b)
; #pragma unroll
;             for (int m = 0; m < 4; ++m)
; #pragma unroll
;                 for (int n = 0; n < 2; ++n) acc[a][b][m][n] = (f32x4){0.f, 0.f, 0.f, 0.f};
;     bf16x8 At[4][2], B0[2][2], B1[2][2]; v8i At8[4], B08[2], B18[2];
;     const char* cA = cur.A; const char* cB = cur.B;
;     PG8_GOFFS(0);
;     PG8_STAGE_B(PG8_SB(0, 0), cB); PG8_STAGE_B(PG8_SB(0, 1), cB + BH); PG8_STAGE_A(PG8_SA(0, 0), cA, 0); PG8_STAGE_A(PG8_SA(0, 1), cA + hstep, 1);
;     if (wr == 1) PG8_BAR;
;     PG8_WAIT_V(2); PG8_BAR;
;     PG8_STAGE_B(PG8_SB(1, 0), cB + kstep); PG8_STAGE_A(PG8_SA(1, 0), cA + kstep, 0); PG8_STAGE_B(PG8_SB(1, 1), cB + BH + kstep);
;     PG8_WAIT_V(6); PG8_BAR;
.LBB0_343:
	v_and_b32_e32 v0, 15, v184
	v_lshlrev_b32_e32 v3, 2, v184
	v_and_b32_e32 v1, 48, v184
	v_lshlrev_b32_e32 v0, 6, v0
	v_and_b32_e32 v3, 32, v3
	s_lshl_b32 s20, s20, 12
	v_or_b32_e32 v2, v0, v1
	v_bitop3_b32 v0, v0, v3, v1 bitop3:0x36
	s_and_b32 s20, s20, 0x3000
	v_mov_b32_e32 v152, v97
	v_or_b32_e32 v100, s20, v0
	s_waitcnt vmcnt(2)
	s_barrier
	s_add_i32 m0, s25, 0x18000
	v_lshl_add_u64 v[0:1], s[8:9], 0, v[152:153]
	v_lshl_add_u64 v[0:1], v[0:1], 0, s[34:35]
	v_mov_b32_e32 v152, v99
	global_load_lds_dwordx4 v[0:1], off
	s_add_i32 m0, s25, 0x1a000
	v_lshl_add_u64 v[0:1], s[8:9], 0, v[152:153]
	v_lshl_add_u64 v[0:1], v[0:1], 0, s[34:35]
	v_mov_b32_e32 v152, v96
	global_load_lds_dwordx4 v[0:1], off
	s_add_i32 s30, s25, 0x8000
	v_lshl_add_u64 v[0:1], s[12:13], 0, v[152:153]
	v_lshl_add_u64 v[0:1], v[0:1], 0, s[34:35]
	s_mov_b32 m0, s30
	v_mov_b32_e32 v152, v98
	global_load_lds_dwordx4 v[0:1], off
	s_add_i32 s31, s25, 0xa000
	v_lshl_add_u64 v[0:1], s[12:13], 0, v[152:153]
	s_lshl_b32 s18, s18, 13
	v_lshl_add_u64 v[0:1], v[0:1], 0, s[34:35]
	s_mov_b32 m0, s31
	s_add_u32 s20, s8, 0x40080
	global_load_lds_dwordx4 v[0:1], off
	v_mov_b32_e32 v0, v97
	s_addc_u32 s21, s9, 0
	s_add_i32 m0, s25, 0x1c000
	v_bitop3_b32 v2, v2, s18, v3 bitop3:0xde
	global_load_lds_dwordx4 v0, s[20:21]
	v_mov_b32_e32 v0, v99
	s_add_i32 m0, s25, 0x1e000
	s_add_u32 s33, s4, s16
	global_load_lds_dwordx4 v0, s[20:21]
	s_addc_u32 s40, s5, s17
	s_add_u32 s14, s14, s19
	s_addc_u32 s15, s15, 0
	s_add_u32 s14, s4, s14
	s_waitcnt vmcnt(6)
	s_addc_u32 s15, s5, s15
	s_add_u32 s41, s14, 0x1b00100
	v_mov_b32_e32 v0, 0
	s_addc_u32 s57, s15, 0
	s_mov_b32 s58, -2
	s_mov_b64 s[14:15], 0
	v_add_u32_e32 v101, 0, v2
	v_mov_b32_e32 v1, 0
	v_mov_b64_e32 v[2:3], 0
	v_mov_b64_e32 v[4:5], 0
	v_mov_b64_e32 v[6:7], 0
	v_mov_b64_e32 v[8:9], 0
	v_mov_b64_e32 v[10:11], 0
	v_mov_b64_e32 v[12:13], 0
	v_mov_b64_e32 v[14:15], 0
	v_mov_b64_e32 v[16:17], 0
	v_mov_b64_e32 v[18:19], 0
	v_mov_b64_e32 v[20:21], 0
	v_mov_b64_e32 v[22:23], 0
	v_mov_b64_e32 v[24:25], 0
	v_mov_b64_e32 v[26:27], 0
	v_mov_b64_e32 v[28:29], 0
	v_mov_b64_e32 v[30:31], 0
	v_mov_b64_e32 v[64:65], 0
	v_mov_b64_e32 v[66:67], 0
	v_mov_b64_e32 v[68:69], 0
	v_mov_b64_e32 v[70:71], 0
	v_mov_b64_e32 v[72:73], 0
	v_mov_b64_e32 v[74:75], 0
	v_mov_b64_e32 v[76:77], 0
	v_mov_b64_e32 v[78:79], 0
	v_mov_b64_e32 v[80:81], 0
	v_mov_b64_e32 v[82:83], 0
	v_mov_b64_e32 v[84:85], 0
	v_mov_b64_e32 v[86:87], 0
	v_mov_b64_e32 v[88:89], 0
	v_mov_b64_e32 v[90:91], 0
	v_mov_b64_e32 v[92:93], 0
	v_mov_b64_e32 v[94:95], 0
	v_mov_b64_e32 v[32:33], 0
	v_mov_b64_e32 v[34:35], 0
	v_mov_b64_e32 v[36:37], 0
	v_mov_b64_e32 v[38:39], 0
	v_mov_b64_e32 v[40:41], 0
	v_mov_b64_e32 v[42:43], 0
	v_mov_b64_e32 v[44:45], 0
	v_mov_b64_e32 v[46:47], 0
	v_mov_b64_e32 v[48:49], 0
	v_mov_b64_e32 v[50:51], 0
	v_mov_b64_e32 v[52:53], 0
	v_mov_b64_e32 v[54:55], 0
	v_mov_b64_e32 v[56:57], 0
	v_mov_b64_e32 v[58:59], 0
	v_mov_b64_e32 v[60:61], 0
	v_mov_b64_e32 v[62:63], 0
	v_mov_b64_e32 v[104:105], 0
	v_mov_b64_e32 v[106:107], 0
	v_mov_b64_e32 v[108:109], 0
	v_mov_b64_e32 v[110:111], 0
	v_mov_b64_e32 v[112:113], 0
	v_mov_b64_e32 v[114:115], 0
	v_mov_b64_e32 v[116:117], 0
	v_mov_b64_e32 v[118:119], 0
	v_mov_b64_e32 v[120:121], 0
	v_mov_b64_e32 v[122:123], 0
	v_mov_b64_e32 v[124:125], 0
	v_mov_b64_e32 v[126:127], 0
	v_mov_b64_e32 v[128:129], 0
	v_mov_b64_e32 v[130:131], 0
	v_mov_b64_e32 v[132:133], 0
	v_mov_b64_e32 v[134:135], 0
	s_barrier

; #define PG8_BAR __builtin_amdgcn_s_barrier()
; template <int K, bool PERM, bool GATHER, int MODE  , class Sched, class Epi>
; __device__ __forceinline__ void gemm_phase(LAS unsigned char* lds, const Sched& S, const Epi& E, const LAS int* gtab, int wv) {
;     ...
;         if (!has_next) break;
; #pragma unroll
;         for (int a = 0; a < 2; ++a)
; #pragma unroll
;             for (int b = 0; b < 2; ++b)
; #pragma unroll
;                 for (int m = 0; m < 4; ++m)
; #pragma unroll
;                     for (int n = 0; n < 2; ++n) acc[a][b][m][n] = (f32x4){0.f, 0.f, 0.f, 0.f};
;         pmt = cur.r0 >> 8; cur = nxt; cA = nA; cB = nB; ++ui;
;         if (wr == 1) PG8_BAR;
.LBB0_364:
	s_add_u32 s14, s14, 0x20080
	s_addc_u32 s15, s15, 0
	s_add_u32 s67, s16, 0x100
	v_mov_b32_e32 v0, 0
	s_addc_u32 s68, s17, 0
	s_mov_b32 s69, -2
	v_mov_b32_e32 v1, 0
	v_mov_b64_e32 v[2:3], 0
	v_mov_b64_e32 v[4:5], 0
	v_mov_b64_e32 v[6:7], 0
	v_mov_b64_e32 v[8:9], 0
	v_mov_b64_e32 v[10:11], 0
	v_mov_b64_e32 v[12:13], 0
	v_mov_b64_e32 v[14:15], 0
	v_mov_b64_e32 v[16:17], 0
	v_mov_b64_e32 v[18:19], 0
	v_mov_b64_e32 v[20:21], 0
	v_mov_b64_e32 v[22:23], 0
	v_mov_b64_e32 v[24:25], 0
	v_mov_b64_e32 v[26:27], 0
	v_mov_b64_e32 v[28:29], 0
	v_mov_b64_e32 v[30:31], 0
	v_mov_b64_e32 v[60:61], 0
	v_mov_b64_e32 v[62:63], 0
	v_mov_b64_e32 v[68:69], 0
	v_mov_b64_e32 v[70:71], 0
	v_mov_b64_e32 v[72:73], 0
	v_mov_b64_e32 v[74:75], 0
	v_mov_b64_e32 v[76:77], 0
	v_mov_b64_e32 v[78:79], 0
	v_mov_b64_e32 v[80:81], 0
	v_mov_b64_e32 v[82:83], 0
	v_mov_b64_e32 v[84:85], 0
	v_mov_b64_e32 v[86:87], 0
	v_mov_b64_e32 v[88:89], 0
	v_mov_b64_e32 v[90:91], 0
	v_mov_b64_e32 v[92:93], 0
	v_mov_b64_e32 v[94:95], 0
	v_mov_b64_e32 v[32:33], 0
	v_mov_b64_e32 v[34:35], 0
	v_mov_b64_e32 v[36:37], 0
	v_mov_b64_e32 v[38:39], 0
	v_mov_b64_e32 v[40:41], 0
	v_mov_b64_e32 v[42:43], 0
	v_mov_b64_e32 v[44:45], 0
	v_mov_b64_e32 v[46:47], 0
	v_mov_b64_e32 v[48:49], 0
	v_mov_b64_e32 v[50:51], 0
	v_mov_b64_e32 v[52:53], 0
	v_mov_b64_e32 v[54:55], 0
	v_mov_b64_e32 v[56:57], 0
	v_mov_b64_e32 v[58:59], 0
	v_mov_b64_e32 v[64:65], 0
	v_mov_b64_e32 v[66:67], 0
	v_mov_b64_e32 v[96:97], 0
	v_mov_b64_e32 v[98:99], 0
	v_mov_b64_e32 v[100:101], 0
	v_mov_b64_e32 v[102:103], 0
	v_mov_b64_e32 v[104:105], 0
	v_mov_b64_e32 v[106:107], 0
	v_mov_b64_e32 v[108:109], 0
	v_mov_b64_e32 v[110:111], 0
	v_mov_b64_e32 v[112:113], 0
	v_mov_b64_e32 v[114:115], 0
	v_mov_b64_e32 v[116:117], 0
	v_mov_b64_e32 v[118:119], 0
	v_mov_b64_e32 v[120:121], 0
	v_mov_b64_e32 v[122:123], 0
	v_mov_b64_e32 v[124:125], 0
	v_mov_b64_e32 v[126:127], 0

; #define PG8_STAGE_B(bufoff, gbase) do { _Pragma("unroll") for (int _i = 0; _i < 2; ++_i) { unsigned _o = voffB[_i]; asm volatile("" : "+v"(_o)); \
;         __builtin_amdgcn_global_load_lds((const unsigned*)((const char*)(gbase) + _o), (LAS unsigned*)(lds + (bufoff) + ldsw + _i * 8192), 16, 0, 0); } } while (0)
; #define PG8_STAGE_A(bufoff, gbase, h) do { _Pragma("unroll") for (int _i = 0; _i < 2; ++_i) { unsigned _o = (GATHER ? aoffs[h][_i] : voffA[_i]); asm volatile("" : "+v"(_o)); \
;         __builtin_amdgcn_global_load_lds((const unsigned*)((const char*)(gbase) + _o), (LAS unsigned*)(lds + (bufoff) + ldsw + _i * 8192), 16, 0, 0); } } while (0)
; #define PG8_GOFFS(u) do { if constexpr (GATHER) { _Pragma("unroll") for (int _i = 0; _i < 2; ++_i) { int _R, _C; stage_rc(tid * 16 + _i * 8192, _R, _C); \
;         aoffs[0][_i] = (unsigned)gtab[(u) * 256 + _R] * (unsigned)(K * ES) + (unsigned)(_C * 2); aoffs[1][_i] = (unsigned)gtab[(u) * 256 + 128 + _R] * (unsigned)(K * ES) + (unsigned)(_C * 2); } } } while (0)
; #define PG8_WAIT_V(n) asm volatile("s_waitcnt vmcnt(" #n ")" ::: "memory")
; #define PG8_BAR __builtin_amdgcn_s_barrier()
; template <int K, bool PERM, bool GATHER, int MODE  , class Sched, class Epi>
; __device__ __forceinline__ void gemm_phase(LAS unsigned char* lds, const Sched& S, const Epi& E, const LAS int* gtab, int wv) {
;     ...
;     f32x4 acc[2][2][4][2];
; #pragma unroll
;     for (int a = 0; a < 2; ++a)
; #pragma unroll
;         for (int b = 0; b < 2; ++b)
; #pragma unroll
;             for (int m = 0; m < 4; ++m)
; #pragma unroll
;                 for (int n = 0; n < 2; ++n) acc[a][b][m][n] = (f32x4){0.f, 0.f, 0.f, 0.f};
;     bf16x8 At[4][2], B0[2][2], B1[2][2]; v8i At8[4], B08[2], B18[2];
;     const char* cA = cur.A; const char* cB = cur.B;
;     PG8_GOFFS(0);
;     PG8_STAGE_B(PG8_SB(0, 0), cB); PG8_STAGE_B(PG8_SB(0, 1), cB + BH); PG8_STAGE_A(PG8_SA(0, 0), cA, 0); PG8_STAGE_A(PG8_SA(0, 1), cA + hstep, 1);
;     if (wr == 1) PG8_BAR;
;     PG8_WAIT_V(2); PG8_BAR;
;     PG8_STAGE_B(PG8_SB(1, 0), cB + kstep); PG8_STAGE_A(PG8_SA(1, 0), cA + kstep, 0); PG8_STAGE_B(PG8_SB(1, 1), cB + BH + kstep);
;     PG8_WAIT_V(6); PG8_BAR;
.LBB0_547:
	v_and_b32_e32 v0, 15, v142
	v_lshlrev_b32_e32 v3, 2, v142
	v_and_b32_e32 v1, 48, v142
	v_lshlrev_b32_e32 v0, 6, v0
	v_and_b32_e32 v3, 32, v3
	s_lshl_b32 s23, s23, 12
	v_or_b32_e32 v2, v0, v1
	v_bitop3_b32 v0, v0, v3, v1 bitop3:0x36
	s_and_b32 s23, s23, 0x3000
	v_mov_b32_e32 v152, v97
	v_or_b32_e32 v100, s23, v0
	s_waitcnt vmcnt(2)
	s_barrier
	s_add_i32 m0, s19, 0x18000
	v_lshl_add_u64 v[0:1], s[4:5], 0, v[152:153]
	v_lshl_add_u64 v[0:1], v[0:1], 0, s[34:35]
	v_mov_b32_e32 v152, v99
	global_load_lds_dwordx4 v[0:1], off
	s_add_i32 m0, s19, 0x1a000
	v_lshl_add_u64 v[0:1], s[4:5], 0, v[152:153]
	v_lshl_add_u64 v[0:1], v[0:1], 0, s[34:35]
	v_mov_b32_e32 v152, v96
	global_load_lds_dwordx4 v[0:1], off
	s_add_i32 s23, s19, 0x8000
	v_lshl_add_u64 v[0:1], s[8:9], 0, v[152:153]
	v_lshl_add_u64 v[0:1], v[0:1], 0, s[34:35]
	s_mov_b32 m0, s23
	v_mov_b32_e32 v152, v98
	global_load_lds_dwordx4 v[0:1], off
	s_add_i32 s24, s19, 0xa000
	v_lshl_add_u64 v[0:1], s[8:9], 0, v[152:153]
	s_lshl_b32 s14, s14, 13
	v_lshl_add_u64 v[0:1], v[0:1], 0, s[34:35]
	s_mov_b32 m0, s24
	s_add_u32 s26, s4, 0x40080
	global_load_lds_dwordx4 v[0:1], off
	v_mov_b32_e32 v0, v97
	s_addc_u32 s27, s5, 0
	s_add_i32 m0, s19, 0x1c000
	v_bitop3_b32 v2, v2, s14, v3 bitop3:0xde
	global_load_lds_dwordx4 v0, s[26:27]
	v_mov_b32_e32 v0, v99
	s_add_i32 m0, s19, 0x1e000
	s_add_u32 s25, s0, s12
	global_load_lds_dwordx4 v0, s[26:27]
	s_addc_u32 s26, s1, s13
	s_add_u32 s10, s10, s15
	s_addc_u32 s11, s11, 0
	s_add_u32 s10, s0, s10
	s_waitcnt vmcnt(6)
	s_addc_u32 s11, s1, s11
	s_add_u32 s27, s10, 0x700100
	v_mov_b32_e32 v0, 0
	s_addc_u32 s28, s11, 0
	s_mov_b32 s30, -2
	s_mov_b64 s[10:11], 0
	v_add_u32_e32 v101, 0, v2
	v_mov_b32_e32 v1, 0
	v_mov_b64_e32 v[2:3], 0
	v_mov_b64_e32 v[4:5], 0
	v_mov_b64_e32 v[6:7], 0
	v_mov_b64_e32 v[8:9], 0
	v_mov_b64_e32 v[10:11], 0
	v_mov_b64_e32 v[12:13], 0
	v_mov_b64_e32 v[14:15], 0
	v_mov_b64_e32 v[16:17], 0
	v_mov_b64_e32 v[18:19], 0
	v_mov_b64_e32 v[20:21], 0
	v_mov_b64_e32 v[22:23], 0
	v_mov_b64_e32 v[24:25], 0
	v_mov_b64_e32 v[26:27], 0
	v_mov_b64_e32 v[28:29], 0
	v_mov_b64_e32 v[30:31], 0
	v_mov_b64_e32 v[64:65], 0
	v_mov_b64_e32 v[66:67], 0
	v_mov_b64_e32 v[68:69], 0
	v_mov_b64_e32 v[70:71], 0
	v_mov_b64_e32 v[72:73], 0
	v_mov_b64_e32 v[74:75], 0
	v_mov_b64_e32 v[76:77], 0
	v_mov_b64_e32 v[78:79], 0
	v_mov_b64_e32 v[80:81], 0
	v_mov_b64_e32 v[82:83], 0
	v_mov_b64_e32 v[84:85], 0
	v_mov_b64_e32 v[86:87], 0
	v_mov_b64_e32 v[88:89], 0
	v_mov_b64_e32 v[90:91], 0
	v_mov_b64_e32 v[92:93], 0
	v_mov_b64_e32 v[94:95], 0
	v_mov_b64_e32 v[32:33], 0
	v_mov_b64_e32 v[34:35], 0
	v_mov_b64_e32 v[36:37], 0
	v_mov_b64_e32 v[38:39], 0
	v_mov_b64_e32 v[40:41], 0
	v_mov_b64_e32 v[42:43], 0
	v_mov_b64_e32 v[44:45], 0
	v_mov_b64_e32 v[46:47], 0
	v_mov_b64_e32 v[48:49], 0
	v_mov_b64_e32 v[50:51], 0
	v_mov_b64_e32 v[52:53], 0
	v_mov_b64_e32 v[54:55], 0
	v_mov_b64_e32 v[56:57], 0
	v_mov_b64_e32 v[58:59], 0
	v_mov_b64_e32 v[60:61], 0
	v_mov_b64_e32 v[62:63], 0
	v_mov_b64_e32 v[104:105], 0
	v_mov_b64_e32 v[106:107], 0
	v_mov_b64_e32 v[108:109], 0
	v_mov_b64_e32 v[110:111], 0
	v_mov_b64_e32 v[112:113], 0
	v_mov_b64_e32 v[114:115], 0
	v_mov_b64_e32 v[116:117], 0
	v_mov_b64_e32 v[118:119], 0
	v_mov_b64_e32 v[120:121], 0
	v_mov_b64_e32 v[122:123], 0
	v_mov_b64_e32 v[124:125], 0
	v_mov_b64_e32 v[126:127], 0
	v_mov_b64_e32 v[128:129], 0
	v_mov_b64_e32 v[130:131], 0
	v_mov_b64_e32 v[132:133], 0
	v_mov_b64_e32 v[134:135], 0
	s_barrier

; #define LAS __attribute__((address_space(3)))
; #define PG8_STAGE_B(bufoff, gbase) do { _Pragma("unroll") for (int _i = 0; _i < 2; ++_i) { unsigned _o = voffB[_i]; asm volatile("" : "+v"(_o)); \
;         __builtin_amdgcn_global_load_lds((const unsigned*)((const char*)(gbase) + _o), (LAS unsigned*)(lds + (bufoff) + ldsw + _i * 8192), 16, 0, 0); } } while (0)
; #define PG8_STAGE_A(bufoff, gbase, h) do { _Pragma("unroll") for (int _i = 0; _i < 2; ++_i) { unsigned _o = (GATHER ? aoffs[h][_i] : voffA[_i]); asm volatile("" : "+v"(_o)); \
;         __builtin_amdgcn_global_load_lds((const unsigned*)((const char*)(gbase) + _o), (LAS unsigned*)(lds + (bufoff) + ldsw + _i * 8192), 16, 0, 0); } } while (0)
; #define PG8_WAIT_V(n) asm volatile("s_waitcnt vmcnt(" #n ")" ::: "memory")
; #define PG8_BAR __builtin_amdgcn_s_barrier()
; template <int K, bool PERM, bool GATHER, int MODE  , class Sched, class Epi>
; __device__ __forceinline__ void gemm_phase(LAS unsigned char* lds, const Sched& S, const Epi& E, const LAS int* gtab, int wv) {
;     ...
;     f32x4 acc[2][2][4][2];
; #pragma unroll
;     for (int a = 0; a < 2; ++a)
; #pragma unroll
;         for (int b = 0; b < 2; ++b)
; #pragma unroll
;             for (int m = 0; m < 4; ++m)
; #pragma unroll
;                 for (int n = 0; n < 2; ++n) acc[a][b][m][n] = (f32x4){0.f, 0.f, 0.f, 0.f};
;     bf16x8 At[4][2], B0[2][2], B1[2][2]; v8i At8[4], B08[2], B18[2];
;     const char* cA = cur.A; const char* cB = cur.B;
;     PG8_GOFFS(0);
;     PG8_STAGE_B(PG8_SB(0, 0), cB); PG8_STAGE_B(PG8_SB(0, 1), cB + BH); PG8_STAGE_A(PG8_SA(0, 0), cA, 0); PG8_STAGE_A(PG8_SA(0, 1), cA + hstep, 1);
;     if (wr == 1) PG8_BAR;
;     PG8_WAIT_V(2); PG8_BAR;
;     PG8_STAGE_B(PG8_SB(1, 0), cB + kstep); PG8_STAGE_A(PG8_SA(1, 0), cA + kstep, 0); PG8_STAGE_B(PG8_SB(1, 1), cB + BH + kstep);
;     PG8_WAIT_V(6); PG8_BAR;
;     for (;;) {
;         const bool has_next = S.next(ui + 1, nxt);
; __global__ void __launch_bounds__(NTHR, 2) mk_fwd(Args a) {
;     ...
;             UpSched S{(const LAS int*)(lds + UT_OFF), (const char*)(ws + WS_X1B), (const char*)(ws + WS_WUP) + (size_t)L * NEXP * 2048 * DM};
;             EpiUp E{(unsigned*)(ws + WS_CTL) + CW_UPC + L * UPC_STRIDE, ws + WS_HACT, (const LAS float*)(lds + BIAS_OFF)};
;             pg8::gemm_phase<DM, true, true, FP6_UP ? 3 : 1>(lds, S, E, (const LAS int*)(lds + TAB_OFF), wv);
.LBB0_740:
	s_lshl_b32 s68, s6, 8
	v_readlane_b32 s6, v254, 19
	v_readlane_b32 s7, v254, 20
	s_mulk_i32 s6, 0x140
	s_ashr_i32 s7, s6, 31
	s_lshl_b64 s[6:7], s[6:7], 2
	s_add_u32 s6, s10, s6
	s_addc_u32 s7, s11, s7
	s_add_u32 s69, s6, 0x1c000
	s_addc_u32 s72, s7, 0
	v_and_b32_e32 v0, 15, v154
	s_add_u32 s6, s10, 0x50800000
	v_and_b32_e32 v1, 48, v154
	v_lshlrev_b32_e32 v0, 6, v0
	v_lshlrev_b32_e32 v3, 2, v154
	s_addc_u32 s7, s11, 0
	v_or_b32_e32 v2, v0, v1
	s_lshl_b32 s9, s9, 13
	v_and_b32_e32 v3, 32, v3
	v_bitop3_b32 v2, v2, s9, v3 bitop3:0xde
	s_lshl_b32 s9, s13, 12
	v_bitop3_b32 v0, v0, v3, v1 bitop3:0x36
	s_and_b32 s9, s9, 0x3000
	v_or_b32_e32 v3, s9, v0
	v_lshlrev_b32_e32 v0, 1, v154
	v_mov_b32_e32 v152, v157
	v_and_b32_e32 v165, 8, v0
	s_waitcnt vmcnt(2)
	s_barrier
	s_add_i32 s9, s81, s12
	s_mov_b32 m0, s9
	v_lshl_add_u64 v[0:1], s[18:19], 0, v[152:153]
	v_lshl_add_u64 v[0:1], v[0:1], 0, s[34:35]
	v_mov_b32_e32 v152, v160
	global_load_lds_dwordx4 v[0:1], off
	s_add_i32 m0, s9, 0x2000
	v_lshl_add_u64 v[0:1], s[18:19], 0, v[152:153]
	v_lshl_add_u64 v[0:1], v[0:1], 0, s[34:35]
	s_add_u32 s10, s10, 0x4e000080
	global_load_lds_dwordx4 v[0:1], off
	s_addc_u32 s11, s11, 0
	v_mov_b32_e32 v0, v161
	s_add_i32 s74, s3, 0x8000
	s_mov_b32 m0, s74
	s_add_i32 s75, s3, 0xa000
	global_load_lds_dwordx4 v0, s[10:11]
	v_mov_b32_e32 v0, v163
	s_mov_b32 m0, s75
	v_mov_b32_e32 v24, 0
	global_load_lds_dwordx4 v0, s[10:11]
	s_add_u32 s10, s18, 0x100080
	s_addc_u32 s11, s19, 0
	s_add_i32 s9, s45, s12
	v_mov_b32_e32 v0, v157
	s_mov_b32 m0, s9
	v_add_u32_e32 v168, 0, v2
	global_load_lds_dwordx4 v0, s[10:11]
	v_mov_b32_e32 v0, v160
	s_add_i32 m0, s9, 0x2000
	s_add_i32 s9, 0, 0x10000
	global_load_lds_dwordx4 v0, s[10:11]
	s_waitcnt vmcnt(6)
	v_add_u32_e32 v166, s9, v3
	s_add_i32 s9, 0, 0x14000
	s_cmpk_lt_u32 s8, 0x100
	v_add_u32_e32 v167, s9, v3
	v_add_u32_e32 v169, s81, v3
	v_add_u32_e32 v170, s45, v3
	s_mov_b32 s28, -1
	s_mov_b32 s76, 0
	s_cselect_b64 s[8:9], -1, 0
	s_mov_b32 s84, 0
	v_mov_b32_e32 v25, 0
	v_mov_b64_e32 v[26:27], 0
	v_mov_b64_e32 v[28:29], 0
	v_mov_b64_e32 v[30:31], 0
	v_mov_b64_e32 v[32:33], 0
	v_mov_b64_e32 v[34:35], 0
	v_mov_b64_e32 v[36:37], 0
	v_mov_b64_e32 v[38:39], 0
	v_mov_b64_e32 v[40:41], 0
	v_mov_b64_e32 v[42:43], 0
	v_mov_b64_e32 v[44:45], 0
	v_mov_b64_e32 v[46:47], 0
	v_mov_b64_e32 v[48:49], 0
	v_mov_b64_e32 v[50:51], 0
	v_mov_b64_e32 v[52:53], 0
	v_mov_b64_e32 v[54:55], 0
	v_mov_b64_e32 v[56:57], 0
	v_mov_b64_e32 v[58:59], 0
	v_mov_b64_e32 v[60:61], 0
	v_mov_b64_e32 v[62:63], 0
	v_mov_b64_e32 v[64:65], 0
	v_mov_b64_e32 v[66:67], 0
	v_mov_b64_e32 v[68:69], 0
	v_mov_b64_e32 v[70:71], 0
	v_mov_b64_e32 v[72:73], 0
	v_mov_b64_e32 v[74:75], 0
	v_mov_b64_e32 v[76:77], 0
	v_mov_b64_e32 v[78:79], 0
	v_mov_b64_e32 v[80:81], 0
	v_mov_b64_e32 v[82:83], 0
	v_mov_b64_e32 v[84:85], 0
	v_mov_b64_e32 v[86:87], 0
	v_mov_b64_e32 v[88:89], 0
	v_mov_b64_e32 v[90:91], 0
	v_mov_b64_e32 v[92:93], 0
	v_mov_b64_e32 v[94:95], 0
	v_mov_b64_e32 v[96:97], 0
	v_mov_b64_e32 v[98:99], 0
	v_mov_b64_e32 v[100:101], 0
	v_mov_b64_e32 v[102:103], 0
	v_mov_b64_e32 v[104:105], 0
	v_mov_b64_e32 v[106:107], 0
	v_mov_b64_e32 v[108:109], 0
	v_mov_b64_e32 v[110:111], 0
	v_mov_b64_e32 v[112:113], 0
	v_mov_b64_e32 v[114:115], 0
	v_mov_b64_e32 v[116:117], 0
	v_mov_b64_e32 v[118:119], 0
	v_mov_b64_e32 v[120:121], 0
	v_mov_b64_e32 v[122:123], 0
	v_mov_b64_e32 v[124:125], 0
	v_mov_b64_e32 v[126:127], 0
	v_mov_b64_e32 v[128:129], 0
	v_mov_b64_e32 v[130:131], 0
	v_mov_b64_e32 v[132:133], 0
	v_mov_b64_e32 v[134:135], 0
	v_mov_b64_e32 v[136:137], 0
	v_mov_b64_e32 v[138:139], 0
	v_mov_b64_e32 v[140:141], 0
	v_mov_b64_e32 v[142:143], 0
	v_mov_b64_e32 v[144:145], 0
	v_mov_b64_e32 v[146:147], 0
	v_mov_b64_e32 v[148:149], 0
	v_mov_b64_e32 v[150:151], 0
	s_barrier
	s_add_i32 s79, s84, 1
	s_cmp_gt_i32 s84, 10
	s_mov_b64 s[20:21], 0
	s_cbranch_scc1 .LBB0_743

; #define PG8_BAR __builtin_amdgcn_s_barrier()
; template <int K, bool PERM, bool GATHER, int MODE  , class Sched, class Epi>
; __device__ __forceinline__ void gemm_phase(LAS unsigned char* lds, const Sched& S, const Epi& E, const LAS int* gtab, int wv) {
;     ...
;         if (!has_next) break;
; #pragma unroll
;         for (int a = 0; a < 2; ++a)
; #pragma unroll
;             for (int b = 0; b < 2; ++b)
; #pragma unroll
;                 for (int m = 0; m < 4; ++m)
; #pragma unroll
;                     for (int n = 0; n < 2; ++n) acc[a][b][m][n] = (f32x4){0.f, 0.f, 0.f, 0.f};
;         pmt = cur.r0 >> 8; cur = nxt; cA = nA; cB = nB; ++ui;
;         if (wr == 1) PG8_BAR;
.LBB0_758:
	v_mov_b32_e32 v24, 0
	s_ashr_i32 s28, s68, 8
	s_mov_b32 s68, s11
	s_mov_b32 s2, s10
	s_mov_b32 s76, s77
	s_mov_b64 s[18:19], s[12:13]
	v_mov_b32_e32 v25, 0
	v_mov_b64_e32 v[26:27], 0
	v_mov_b64_e32 v[28:29], 0
	v_mov_b64_e32 v[30:31], 0
	v_mov_b64_e32 v[32:33], 0
	v_mov_b64_e32 v[34:35], 0
	v_mov_b64_e32 v[36:37], 0
	v_mov_b64_e32 v[38:39], 0
	v_mov_b64_e32 v[40:41], 0
	v_mov_b64_e32 v[42:43], 0
	v_mov_b64_e32 v[44:45], 0
	v_mov_b64_e32 v[46:47], 0
	v_mov_b64_e32 v[48:49], 0
	v_mov_b64_e32 v[50:51], 0
	v_mov_b64_e32 v[52:53], 0
	v_mov_b64_e32 v[54:55], 0
	v_mov_b64_e32 v[56:57], 0
	v_mov_b64_e32 v[58:59], 0
	v_mov_b64_e32 v[60:61], 0
	v_mov_b64_e32 v[62:63], 0
	v_mov_b64_e32 v[64:65], 0
	v_mov_b64_e32 v[66:67], 0
	v_mov_b64_e32 v[68:69], 0
	v_mov_b64_e32 v[70:71], 0
	v_mov_b64_e32 v[72:73], 0
	v_mov_b64_e32 v[74:75], 0
	v_mov_b64_e32 v[76:77], 0
	v_mov_b64_e32 v[78:79], 0
	v_mov_b64_e32 v[80:81], 0
	v_mov_b64_e32 v[82:83], 0
	v_mov_b64_e32 v[84:85], 0
	v_mov_b64_e32 v[86:87], 0
	v_mov_b64_e32 v[88:89], 0
	v_mov_b64_e32 v[90:91], 0
	v_mov_b64_e32 v[92:93], 0
	v_mov_b64_e32 v[94:95], 0
	v_mov_b64_e32 v[96:97], 0
	v_mov_b64_e32 v[98:99], 0
	v_mov_b64_e32 v[100:101], 0
	v_mov_b64_e32 v[102:103], 0
	v_mov_b64_e32 v[104:105], 0
	v_mov_b64_e32 v[106:107], 0
	v_mov_b64_e32 v[108:109], 0
	v_mov_b64_e32 v[110:111], 0
	v_mov_b64_e32 v[112:113], 0
	v_mov_b64_e32 v[114:115], 0
	v_mov_b64_e32 v[116:117], 0
	v_mov_b64_e32 v[118:119], 0
	v_mov_b64_e32 v[120:121], 0
	v_mov_b64_e32 v[122:123], 0
	v_mov_b64_e32 v[124:125], 0
	v_mov_b64_e32 v[126:127], 0
	v_mov_b64_e32 v[128:129], 0
	v_mov_b64_e32 v[130:131], 0
	v_mov_b64_e32 v[132:133], 0
	v_mov_b64_e32 v[134:135], 0
	v_mov_b64_e32 v[136:137], 0
	v_mov_b64_e32 v[138:139], 0
	v_mov_b64_e32 v[140:141], 0
	v_mov_b64_e32 v[142:143], 0
	v_mov_b64_e32 v[144:145], 0
	v_mov_b64_e32 v[146:147], 0
	v_mov_b64_e32 v[148:149], 0
	v_mov_b64_e32 v[150:151], 0
	s_andn2_b64 vcc, exec, s[14:15]
	s_cbranch_vccnz .LBB0_760
	s_branch .LBB0_761

; #define PG8_BAR __builtin_amdgcn_s_barrier()
; template <int K, bool PERM, bool GATHER, int MODE  , class Sched, class Epi>
; __device__ __forceinline__ void gemm_phase(LAS unsigned char* lds, const Sched& S, const Epi& E, const LAS int* gtab, int wv) {
;     ...
;         const bool has_next = S.next(ui + 1, nxt);
;         const char* nA = has_next ? nxt.A : cA; const char* nB = has_next ? nxt.B : cB;
;     ...
;         if (!has_next) break;
; #pragma unroll
;         for (int a = 0; a < 2; ++a)
; #pragma unroll
;             for (int b = 0; b < 2; ++b)
; #pragma unroll
;                 for (int m = 0; m < 4; ++m)
; #pragma unroll
;                     for (int n = 0; n < 2; ++n) acc[a][b][m][n] = (f32x4){0.f, 0.f, 0.f, 0.f};
;         pmt = cur.r0 >> 8; cur = nxt; cA = nA; cB = nB; ++ui;
;         if (wr == 1) PG8_BAR;
.LBB0_868:
	s_and_b64 s[20:21], s[12:13], exec
	s_cselect_b32 s65, s7, s17
	s_cselect_b32 s66, s6, s16
	s_cselect_b32 s67, s11, s19
	s_cselect_b32 s68, s10, s18
	s_add_u32 s16, s16, 0x20080
	s_addc_u32 s17, s17, 0
	s_add_u32 s69, s18, 0x100
	v_mov_b32_e32 v0, 0
	s_addc_u32 s72, s19, 0
	s_mov_b32 s73, -2
	v_mov_b32_e32 v1, 0
	v_mov_b64_e32 v[2:3], 0
	v_mov_b64_e32 v[4:5], 0
	v_mov_b64_e32 v[6:7], 0
	v_mov_b64_e32 v[8:9], 0
	v_mov_b64_e32 v[10:11], 0
	v_mov_b64_e32 v[12:13], 0
	v_mov_b64_e32 v[14:15], 0
	v_mov_b64_e32 v[16:17], 0
	v_mov_b64_e32 v[18:19], 0
	v_mov_b64_e32 v[20:21], 0
	v_mov_b64_e32 v[22:23], 0
	v_mov_b64_e32 v[24:25], 0
	v_mov_b64_e32 v[26:27], 0
	v_mov_b64_e32 v[28:29], 0
	v_mov_b64_e32 v[30:31], 0
	v_mov_b64_e32 v[64:65], 0
	v_mov_b64_e32 v[66:67], 0
	v_mov_b64_e32 v[68:69], 0
	v_mov_b64_e32 v[70:71], 0
	v_mov_b64_e32 v[72:73], 0
	v_mov_b64_e32 v[74:75], 0
	v_mov_b64_e32 v[76:77], 0
	v_mov_b64_e32 v[78:79], 0
	v_mov_b64_e32 v[80:81], 0
	v_mov_b64_e32 v[82:83], 0
	v_mov_b64_e32 v[84:85], 0
	v_mov_b64_e32 v[86:87], 0
	v_mov_b64_e32 v[88:89], 0
	v_mov_b64_e32 v[90:91], 0
	v_mov_b64_e32 v[92:93], 0
	v_mov_b64_e32 v[94:95], 0
	v_mov_b64_e32 v[32:33], 0
	v_mov_b64_e32 v[34:35], 0
	v_mov_b64_e32 v[36:37], 0
	v_mov_b64_e32 v[38:39], 0
	v_mov_b64_e32 v[40:41], 0
	v_mov_b64_e32 v[42:43], 0
	v_mov_b64_e32 v[44:45], 0
	v_mov_b64_e32 v[46:47], 0
	v_mov_b64_e32 v[48:49], 0
	v_mov_b64_e32 v[50:51], 0
	v_mov_b64_e32 v[52:53], 0
	v_mov_b64_e32 v[54:55], 0
	v_mov_b64_e32 v[56:57], 0
	v_mov_b64_e32 v[58:59], 0
	v_mov_b64_e32 v[60:61], 0
	v_mov_b64_e32 v[62:63], 0
	v_mov_b64_e32 v[96:97], 0
	v_mov_b64_e32 v[98:99], 0
	v_mov_b64_e32 v[100:101], 0
	v_mov_b64_e32 v[102:103], 0
	v_mov_b64_e32 v[104:105], 0
	v_mov_b64_e32 v[106:107], 0
	v_mov_b64_e32 v[108:109], 0
	v_mov_b64_e32 v[110:111], 0
	v_mov_b64_e32 v[112:113], 0
	v_mov_b64_e32 v[114:115], 0
	v_mov_b64_e32 v[116:117], 0
	v_mov_b64_e32 v[118:119], 0
	v_mov_b64_e32 v[120:121], 0
	v_mov_b64_e32 v[122:123], 0
	v_mov_b64_e32 v[124:125], 0
	v_mov_b64_e32 v[126:127], 0
